# gate|up epilogue: hazard pads placed behind the address setup instead of in front of it
# baseline (speedup 1.0000x reference)
.LBB0_996:
	s_ashr_i32 s6, s13, 1
	v_add_u32_e32 v8, s10, v233
	v_add_u32_e32 v2, s6, v235
	v_mov_b64_e32 v[4:5], s[22:23]
	s_movk_i32 s8, 0x600
	v_ashrrev_i32_e32 v3, 31, v2
	s_and_b64 vcc, exec, s[58:59]
	s_mov_b32 s13, s73
	s_mov_b32 s10, s44
	s_mov_b64 s[26:27], s[56:57]
	s_mov_b32 s100, 0xbfb8aa3b
	s_mov_b32 s101, 0x41000000
	v_mad_i64_i32 v[6:7], s[6:7], v8, s8, v[4:5]
	v_add_u32_e32 v9, 16, v8
	v_mad_i64_i32 v[46:47], s[6:7], v9, s8, v[4:5]
	s_nop 15
	s_nop 15
	v_pk_mul_f32 v[18:19], v[190:191], s[100:101] op_sel_hi:[1,0]
	v_pk_mul_f32 v[20:21], v[192:193], s[100:101] op_sel_hi:[1,0]
	v_pk_mul_f32 v[22:23], v[182:183], s[100:101] op_sel_hi:[1,0]
	v_pk_mul_f32 v[24:25], v[184:185], s[100:101] op_sel_hi:[1,0]
	v_pk_mul_f32 v[26:27], v[174:175], s[100:101] op_sel_hi:[1,0]
	v_pk_mul_f32 v[28:29], v[176:177], s[100:101] op_sel_hi:[1,0]
	v_pk_mul_f32 v[30:31], v[166:167], s[100:101] op_sel_hi:[1,0]
	v_pk_mul_f32 v[32:33], v[168:169], s[100:101] op_sel_hi:[1,0]
	v_lshl_add_u64 v[6:7], v[6:7], 0, v[2:3]
	v_lshl_add_u64 v[46:47], v[46:47], 0, v[2:3]
	v_exp_f32_e32 v18, v18
	v_exp_f32_e32 v19, v19
	v_exp_f32_e32 v20, v20
	v_exp_f32_e32 v21, v21
	v_exp_f32_e32 v22, v22
	v_exp_f32_e32 v23, v23
	v_exp_f32_e32 v24, v24
	v_exp_f32_e32 v25, v25
	v_exp_f32_e32 v26, v26
	v_exp_f32_e32 v27, v27
	v_exp_f32_e32 v28, v28
	v_exp_f32_e32 v29, v29
	v_exp_f32_e32 v30, v30
	v_exp_f32_e32 v31, v31
	v_exp_f32_e32 v32, v32
	v_exp_f32_e32 v33, v33
	v_pk_add_f32 v[18:19], v[18:19], 1.0 op_sel_hi:[1,0]
	v_pk_add_f32 v[20:21], v[20:21], 1.0 op_sel_hi:[1,0]
	v_pk_add_f32 v[22:23], v[22:23], 1.0 op_sel_hi:[1,0]
	v_pk_add_f32 v[24:25], v[24:25], 1.0 op_sel_hi:[1,0]
	v_pk_add_f32 v[26:27], v[26:27], 1.0 op_sel_hi:[1,0]
	v_pk_add_f32 v[28:29], v[28:29], 1.0 op_sel_hi:[1,0]
	v_pk_add_f32 v[30:31], v[30:31], 1.0 op_sel_hi:[1,0]
	v_pk_add_f32 v[32:33], v[32:33], 1.0 op_sel_hi:[1,0]
	v_rcp_f32_e32 v18, v18
	v_rcp_f32_e32 v19, v19
	v_rcp_f32_e32 v20, v20
	v_rcp_f32_e32 v21, v21
	v_rcp_f32_e32 v22, v22
	v_rcp_f32_e32 v23, v23
	v_rcp_f32_e32 v24, v24
	v_rcp_f32_e32 v25, v25
	v_rcp_f32_e32 v26, v26
	v_rcp_f32_e32 v27, v27
	v_rcp_f32_e32 v28, v28
	v_rcp_f32_e32 v29, v29
	v_rcp_f32_e32 v30, v30
	v_rcp_f32_e32 v31, v31
	v_rcp_f32_e32 v32, v32
	v_rcp_f32_e32 v33, v33
	v_pk_mul_f32 v[18:19], v[190:191], v[18:19]
	v_pk_mul_f32 v[20:21], v[192:193], v[20:21]
	v_pk_mul_f32 v[22:23], v[182:183], v[22:23]
	v_pk_mul_f32 v[24:25], v[184:185], v[24:25]
	v_pk_mul_f32 v[26:27], v[174:175], v[26:27]
	v_pk_mul_f32 v[28:29], v[176:177], v[28:29]
	v_pk_mul_f32 v[30:31], v[166:167], v[30:31]
	v_pk_mul_f32 v[32:33], v[168:169], v[32:33]
	v_pk_mul_f32 v[18:19], v[18:19], v[186:187]
	v_pk_mul_f32 v[20:21], v[20:21], v[188:189]
	v_pk_mul_f32 v[22:23], v[22:23], v[178:179]
	v_pk_mul_f32 v[24:25], v[24:25], v[180:181]
	v_pk_mul_f32 v[26:27], v[26:27], v[170:171]
	v_pk_mul_f32 v[28:29], v[28:29], v[172:173]
	v_pk_mul_f32 v[30:31], v[30:31], v[162:163]
	v_pk_mul_f32 v[32:33], v[32:33], v[164:165]
	v_pk_mul_f32 v[18:19], v[18:19], s[100:101] op_sel:[0,1] op_sel_hi:[1,1]
	v_pk_mul_f32 v[20:21], v[20:21], s[100:101] op_sel:[0,1] op_sel_hi:[1,1]
	v_pk_mul_f32 v[22:23], v[22:23], s[100:101] op_sel:[0,1] op_sel_hi:[1,1]
	v_pk_mul_f32 v[24:25], v[24:25], s[100:101] op_sel:[0,1] op_sel_hi:[1,1]
	v_pk_mul_f32 v[26:27], v[26:27], s[100:101] op_sel:[0,1] op_sel_hi:[1,1]
	v_pk_mul_f32 v[28:29], v[28:29], s[100:101] op_sel:[0,1] op_sel_hi:[1,1]
	v_pk_mul_f32 v[30:31], v[30:31], s[100:101] op_sel:[0,1] op_sel_hi:[1,1]
	v_pk_mul_f32 v[32:33], v[32:33], s[100:101] op_sel:[0,1] op_sel_hi:[1,1]
	v_cvt_pk_fp8_f32 v10, v18, v19
	v_cvt_pk_fp8_f32 v12, v26, v27
	v_cvt_pk_fp8_f32 v10, v20, v21 op_sel:[0,0,1]
	v_cvt_pk_fp8_f32 v12, v28, v29 op_sel:[0,0,1]
	v_cvt_pk_fp8_f32 v11, v22, v23
	v_cvt_pk_fp8_f32 v13, v30, v31
	v_cvt_pk_fp8_f32 v11, v24, v25 op_sel:[0,0,1]
	v_cvt_pk_fp8_f32 v13, v32, v33 op_sel:[0,0,1]
	s_nop 0
	global_store_dwordx2 v[6:7], v[10:11], off
	global_store_dwordx2 v[46:47], v[12:13], off
	v_add_u32_e32 v9, 32, v8
	v_mad_i64_i32 v[6:7], s[6:7], v9, s8, v[4:5]
	v_add_u32_e32 v9, 48, v8
	v_mad_i64_i32 v[46:47], s[6:7], v9, s8, v[4:5]
	v_pk_mul_f32 v[18:19], v[158:159], s[100:101] op_sel_hi:[1,0]
	v_pk_mul_f32 v[20:21], v[160:161], s[100:101] op_sel_hi:[1,0]
	v_pk_mul_f32 v[22:23], v[150:151], s[100:101] op_sel_hi:[1,0]
	v_pk_mul_f32 v[24:25], v[152:153], s[100:101] op_sel_hi:[1,0]
	v_pk_mul_f32 v[26:27], v[142:143], s[100:101] op_sel_hi:[1,0]
	v_pk_mul_f32 v[28:29], v[144:145], s[100:101] op_sel_hi:[1,0]
	v_pk_mul_f32 v[30:31], v[134:135], s[100:101] op_sel_hi:[1,0]
	v_pk_mul_f32 v[32:33], v[136:137], s[100:101] op_sel_hi:[1,0]
	v_lshl_add_u64 v[6:7], v[6:7], 0, v[2:3]
	v_lshl_add_u64 v[46:47], v[46:47], 0, v[2:3]
	v_exp_f32_e32 v18, v18
	v_exp_f32_e32 v19, v19
	v_exp_f32_e32 v20, v20
	v_exp_f32_e32 v21, v21
	v_exp_f32_e32 v22, v22
	v_exp_f32_e32 v23, v23
	v_exp_f32_e32 v24, v24
	v_exp_f32_e32 v25, v25
	v_exp_f32_e32 v26, v26
	v_exp_f32_e32 v27, v27
	v_exp_f32_e32 v28, v28
	v_exp_f32_e32 v29, v29
	v_exp_f32_e32 v30, v30
	v_exp_f32_e32 v31, v31
	v_exp_f32_e32 v32, v32
	v_exp_f32_e32 v33, v33
	v_pk_add_f32 v[18:19], v[18:19], 1.0 op_sel_hi:[1,0]
	v_pk_add_f32 v[20:21], v[20:21], 1.0 op_sel_hi:[1,0]
	v_pk_add_f32 v[22:23], v[22:23], 1.0 op_sel_hi:[1,0]
	v_pk_add_f32 v[24:25], v[24:25], 1.0 op_sel_hi:[1,0]
	v_pk_add_f32 v[26:27], v[26:27], 1.0 op_sel_hi:[1,0]
	v_pk_add_f32 v[28:29], v[28:29], 1.0 op_sel_hi:[1,0]
	v_pk_add_f32 v[30:31], v[30:31], 1.0 op_sel_hi:[1,0]
	v_pk_add_f32 v[32:33], v[32:33], 1.0 op_sel_hi:[1,0]
	v_rcp_f32_e32 v18, v18
	v_rcp_f32_e32 v19, v19
	v_rcp_f32_e32 v20, v20
	v_rcp_f32_e32 v21, v21
	v_rcp_f32_e32 v22, v22
	v_rcp_f32_e32 v23, v23
	v_rcp_f32_e32 v24, v24
	v_rcp_f32_e32 v25, v25
	v_rcp_f32_e32 v26, v26
	v_rcp_f32_e32 v27, v27
	v_rcp_f32_e32 v28, v28
	v_rcp_f32_e32 v29, v29
	v_rcp_f32_e32 v30, v30
	v_rcp_f32_e32 v31, v31
	v_rcp_f32_e32 v32, v32
	v_rcp_f32_e32 v33, v33
	v_pk_mul_f32 v[18:19], v[158:159], v[18:19]
	v_pk_mul_f32 v[20:21], v[160:161], v[20:21]
	v_pk_mul_f32 v[22:23], v[150:151], v[22:23]
	v_pk_mul_f32 v[24:25], v[152:153], v[24:25]
	v_pk_mul_f32 v[26:27], v[142:143], v[26:27]
	v_pk_mul_f32 v[28:29], v[144:145], v[28:29]
	v_pk_mul_f32 v[30:31], v[134:135], v[30:31]
	v_pk_mul_f32 v[32:33], v[136:137], v[32:33]
	v_pk_mul_f32 v[18:19], v[18:19], v[154:155]
	v_pk_mul_f32 v[20:21], v[20:21], v[156:157]
	v_pk_mul_f32 v[22:23], v[22:23], v[146:147]
	v_pk_mul_f32 v[24:25], v[24:25], v[148:149]
	v_pk_mul_f32 v[26:27], v[26:27], v[138:139]
	v_pk_mul_f32 v[28:29], v[28:29], v[140:141]
	v_pk_mul_f32 v[30:31], v[30:31], v[130:131]
	v_pk_mul_f32 v[32:33], v[32:33], v[132:133]
	v_pk_mul_f32 v[18:19], v[18:19], s[100:101] op_sel:[0,1] op_sel_hi:[1,1]
	v_pk_mul_f32 v[20:21], v[20:21], s[100:101] op_sel:[0,1] op_sel_hi:[1,1]
	v_pk_mul_f32 v[22:23], v[22:23], s[100:101] op_sel:[0,1] op_sel_hi:[1,1]
	v_pk_mul_f32 v[24:25], v[24:25], s[100:101] op_sel:[0,1] op_sel_hi:[1,1]
	v_pk_mul_f32 v[26:27], v[26:27], s[100:101] op_sel:[0,1] op_sel_hi:[1,1]
	v_pk_mul_f32 v[28:29], v[28:29], s[100:101] op_sel:[0,1] op_sel_hi:[1,1]
	v_pk_mul_f32 v[30:31], v[30:31], s[100:101] op_sel:[0,1] op_sel_hi:[1,1]
	v_pk_mul_f32 v[32:33], v[32:33], s[100:101] op_sel:[0,1] op_sel_hi:[1,1]
	v_cvt_pk_fp8_f32 v10, v18, v19
	v_cvt_pk_fp8_f32 v12, v26, v27
	v_cvt_pk_fp8_f32 v10, v20, v21 op_sel:[0,0,1]
	v_cvt_pk_fp8_f32 v12, v28, v29 op_sel:[0,0,1]
	v_cvt_pk_fp8_f32 v11, v22, v23
	v_cvt_pk_fp8_f32 v13, v30, v31
	v_cvt_pk_fp8_f32 v11, v24, v25 op_sel:[0,0,1]
	v_cvt_pk_fp8_f32 v13, v32, v33 op_sel:[0,0,1]
	s_nop 0
	global_store_dwordx2 v[6:7], v[10:11], off
	global_store_dwordx2 v[46:47], v[12:13], off
	v_add_u32_e32 v9, 0x80, v8
	v_mad_i64_i32 v[6:7], s[6:7], v9, s8, v[4:5]
	v_add_u32_e32 v9, 0x90, v8
	v_mad_i64_i32 v[46:47], s[6:7], v9, s8, v[4:5]
	v_pk_mul_f32 v[18:19], v[126:127], s[100:101] op_sel_hi:[1,0]
	v_pk_mul_f32 v[20:21], v[128:129], s[100:101] op_sel_hi:[1,0]
	v_pk_mul_f32 v[22:23], v[118:119], s[100:101] op_sel_hi:[1,0]
	v_pk_mul_f32 v[24:25], v[120:121], s[100:101] op_sel_hi:[1,0]
	v_pk_mul_f32 v[26:27], v[110:111], s[100:101] op_sel_hi:[1,0]
	v_pk_mul_f32 v[28:29], v[112:113], s[100:101] op_sel_hi:[1,0]
	v_pk_mul_f32 v[30:31], v[102:103], s[100:101] op_sel_hi:[1,0]
	v_pk_mul_f32 v[32:33], v[104:105], s[100:101] op_sel_hi:[1,0]
	v_lshl_add_u64 v[6:7], v[6:7], 0, v[2:3]
	v_lshl_add_u64 v[46:47], v[46:47], 0, v[2:3]
	v_exp_f32_e32 v18, v18
	v_exp_f32_e32 v19, v19
	v_exp_f32_e32 v20, v20
	v_exp_f32_e32 v21, v21
	v_exp_f32_e32 v22, v22
	v_exp_f32_e32 v23, v23
	v_exp_f32_e32 v24, v24
	v_exp_f32_e32 v25, v25
	v_exp_f32_e32 v26, v26
	v_exp_f32_e32 v27, v27
	v_exp_f32_e32 v28, v28
	v_exp_f32_e32 v29, v29
	v_exp_f32_e32 v30, v30
	v_exp_f32_e32 v31, v31
	v_exp_f32_e32 v32, v32
	v_exp_f32_e32 v33, v33
	v_pk_add_f32 v[18:19], v[18:19], 1.0 op_sel_hi:[1,0]
	v_pk_add_f32 v[20:21], v[20:21], 1.0 op_sel_hi:[1,0]
	v_pk_add_f32 v[22:23], v[22:23], 1.0 op_sel_hi:[1,0]
	v_pk_add_f32 v[24:25], v[24:25], 1.0 op_sel_hi:[1,0]
	v_pk_add_f32 v[26:27], v[26:27], 1.0 op_sel_hi:[1,0]
	v_pk_add_f32 v[28:29], v[28:29], 1.0 op_sel_hi:[1,0]
	v_pk_add_f32 v[30:31], v[30:31], 1.0 op_sel_hi:[1,0]
	v_pk_add_f32 v[32:33], v[32:33], 1.0 op_sel_hi:[1,0]
	v_rcp_f32_e32 v18, v18
	v_rcp_f32_e32 v19, v19
	v_rcp_f32_e32 v20, v20
	v_rcp_f32_e32 v21, v21
	v_rcp_f32_e32 v22, v22
	v_rcp_f32_e32 v23, v23
	v_rcp_f32_e32 v24, v24
	v_rcp_f32_e32 v25, v25
	v_rcp_f32_e32 v26, v26
	v_rcp_f32_e32 v27, v27
	v_rcp_f32_e32 v28, v28
	v_rcp_f32_e32 v29, v29
	v_rcp_f32_e32 v30, v30
	v_rcp_f32_e32 v31, v31
	v_rcp_f32_e32 v32, v32
	v_rcp_f32_e32 v33, v33
	v_pk_mul_f32 v[18:19], v[126:127], v[18:19]
	v_pk_mul_f32 v[20:21], v[128:129], v[20:21]
	v_pk_mul_f32 v[22:23], v[118:119], v[22:23]
	v_pk_mul_f32 v[24:25], v[120:121], v[24:25]
	v_pk_mul_f32 v[26:27], v[110:111], v[26:27]
	v_pk_mul_f32 v[28:29], v[112:113], v[28:29]
	v_pk_mul_f32 v[30:31], v[102:103], v[30:31]
	v_pk_mul_f32 v[32:33], v[104:105], v[32:33]
	v_pk_mul_f32 v[18:19], v[18:19], v[122:123]
	v_pk_mul_f32 v[20:21], v[20:21], v[124:125]
	v_pk_mul_f32 v[22:23], v[22:23], v[114:115]
	v_pk_mul_f32 v[24:25], v[24:25], v[116:117]
	v_pk_mul_f32 v[26:27], v[26:27], v[106:107]
	v_pk_mul_f32 v[28:29], v[28:29], v[108:109]
	v_pk_mul_f32 v[30:31], v[30:31], v[98:99]
	v_pk_mul_f32 v[32:33], v[32:33], v[100:101]
	v_pk_mul_f32 v[18:19], v[18:19], s[100:101] op_sel:[0,1] op_sel_hi:[1,1]
	v_pk_mul_f32 v[20:21], v[20:21], s[100:101] op_sel:[0,1] op_sel_hi:[1,1]
	v_pk_mul_f32 v[22:23], v[22:23], s[100:101] op_sel:[0,1] op_sel_hi:[1,1]
	v_pk_mul_f32 v[24:25], v[24:25], s[100:101] op_sel:[0,1] op_sel_hi:[1,1]
	v_pk_mul_f32 v[26:27], v[26:27], s[100:101] op_sel:[0,1] op_sel_hi:[1,1]
	v_pk_mul_f32 v[28:29], v[28:29], s[100:101] op_sel:[0,1] op_sel_hi:[1,1]
	v_pk_mul_f32 v[30:31], v[30:31], s[100:101] op_sel:[0,1] op_sel_hi:[1,1]
	v_pk_mul_f32 v[32:33], v[32:33], s[100:101] op_sel:[0,1] op_sel_hi:[1,1]
	v_cvt_pk_fp8_f32 v10, v18, v19
	v_cvt_pk_fp8_f32 v12, v26, v27
	v_cvt_pk_fp8_f32 v10, v20, v21 op_sel:[0,0,1]
	v_cvt_pk_fp8_f32 v12, v28, v29 op_sel:[0,0,1]
	v_cvt_pk_fp8_f32 v11, v22, v23
	v_cvt_pk_fp8_f32 v13, v30, v31
	v_cvt_pk_fp8_f32 v11, v24, v25 op_sel:[0,0,1]
	v_cvt_pk_fp8_f32 v13, v32, v33 op_sel:[0,0,1]
	s_nop 0
	global_store_dwordx2 v[6:7], v[10:11], off
	global_store_dwordx2 v[46:47], v[12:13], off
	v_add_u32_e32 v9, 0xa0, v8
	v_mad_i64_i32 v[6:7], s[6:7], v9, s8, v[4:5]
	v_add_u32_e32 v9, 0xb0, v8
	v_mad_i64_i32 v[46:47], s[6:7], v9, s8, v[4:5]
	v_pk_mul_f32 v[18:19], v[94:95], s[100:101] op_sel_hi:[1,0]
	v_pk_mul_f32 v[20:21], v[96:97], s[100:101] op_sel_hi:[1,0]
	v_pk_mul_f32 v[22:23], v[86:87], s[100:101] op_sel_hi:[1,0]
	v_pk_mul_f32 v[24:25], v[88:89], s[100:101] op_sel_hi:[1,0]
	v_pk_mul_f32 v[26:27], v[78:79], s[100:101] op_sel_hi:[1,0]
	v_pk_mul_f32 v[28:29], v[80:81], s[100:101] op_sel_hi:[1,0]
	v_pk_mul_f32 v[30:31], v[70:71], s[100:101] op_sel_hi:[1,0]
	v_pk_mul_f32 v[32:33], v[72:73], s[100:101] op_sel_hi:[1,0]
	v_lshl_add_u64 v[6:7], v[6:7], 0, v[2:3]
	v_lshl_add_u64 v[46:47], v[46:47], 0, v[2:3]
	v_exp_f32_e32 v18, v18
	v_exp_f32_e32 v19, v19
	v_exp_f32_e32 v20, v20
	v_exp_f32_e32 v21, v21
	v_exp_f32_e32 v22, v22
	v_exp_f32_e32 v23, v23
	v_exp_f32_e32 v24, v24
	v_exp_f32_e32 v25, v25
	v_exp_f32_e32 v26, v26
	v_exp_f32_e32 v27, v27
	v_exp_f32_e32 v28, v28
	v_exp_f32_e32 v29, v29
	v_exp_f32_e32 v30, v30
	v_exp_f32_e32 v31, v31
	v_exp_f32_e32 v32, v32
	v_exp_f32_e32 v33, v33
	v_pk_add_f32 v[18:19], v[18:19], 1.0 op_sel_hi:[1,0]
	v_pk_add_f32 v[20:21], v[20:21], 1.0 op_sel_hi:[1,0]
	v_pk_add_f32 v[22:23], v[22:23], 1.0 op_sel_hi:[1,0]
	v_pk_add_f32 v[24:25], v[24:25], 1.0 op_sel_hi:[1,0]
	v_pk_add_f32 v[26:27], v[26:27], 1.0 op_sel_hi:[1,0]
	v_pk_add_f32 v[28:29], v[28:29], 1.0 op_sel_hi:[1,0]
	v_pk_add_f32 v[30:31], v[30:31], 1.0 op_sel_hi:[1,0]
	v_pk_add_f32 v[32:33], v[32:33], 1.0 op_sel_hi:[1,0]
	v_rcp_f32_e32 v18, v18
	v_rcp_f32_e32 v19, v19
	v_rcp_f32_e32 v20, v20
	v_rcp_f32_e32 v21, v21
	v_rcp_f32_e32 v22, v22
	v_rcp_f32_e32 v23, v23
	v_rcp_f32_e32 v24, v24
	v_rcp_f32_e32 v25, v25
	v_rcp_f32_e32 v26, v26
	v_rcp_f32_e32 v27, v27
	v_rcp_f32_e32 v28, v28
	v_rcp_f32_e32 v29, v29
	v_rcp_f32_e32 v30, v30
	v_rcp_f32_e32 v31, v31
	v_rcp_f32_e32 v32, v32
	v_rcp_f32_e32 v33, v33
	v_pk_mul_f32 v[18:19], v[94:95], v[18:19]
	v_pk_mul_f32 v[20:21], v[96:97], v[20:21]
	v_pk_mul_f32 v[22:23], v[86:87], v[22:23]
	v_pk_mul_f32 v[24:25], v[88:89], v[24:25]
	v_pk_mul_f32 v[26:27], v[78:79], v[26:27]
	v_pk_mul_f32 v[28:29], v[80:81], v[28:29]
	v_pk_mul_f32 v[30:31], v[70:71], v[30:31]
	v_pk_mul_f32 v[32:33], v[72:73], v[32:33]
	v_pk_mul_f32 v[18:19], v[18:19], v[90:91]
	v_pk_mul_f32 v[20:21], v[20:21], v[92:93]
	v_pk_mul_f32 v[22:23], v[22:23], v[82:83]
	v_pk_mul_f32 v[24:25], v[24:25], v[84:85]
	v_pk_mul_f32 v[26:27], v[26:27], v[74:75]
	v_pk_mul_f32 v[28:29], v[28:29], v[76:77]
	v_pk_mul_f32 v[30:31], v[30:31], v[66:67]
	v_pk_mul_f32 v[32:33], v[32:33], v[68:69]
	v_pk_mul_f32 v[18:19], v[18:19], s[100:101] op_sel:[0,1] op_sel_hi:[1,1]
	v_pk_mul_f32 v[20:21], v[20:21], s[100:101] op_sel:[0,1] op_sel_hi:[1,1]
	v_pk_mul_f32 v[22:23], v[22:23], s[100:101] op_sel:[0,1] op_sel_hi:[1,1]
	v_pk_mul_f32 v[24:25], v[24:25], s[100:101] op_sel:[0,1] op_sel_hi:[1,1]
	v_pk_mul_f32 v[26:27], v[26:27], s[100:101] op_sel:[0,1] op_sel_hi:[1,1]
	v_pk_mul_f32 v[28:29], v[28:29], s[100:101] op_sel:[0,1] op_sel_hi:[1,1]
	v_pk_mul_f32 v[30:31], v[30:31], s[100:101] op_sel:[0,1] op_sel_hi:[1,1]
	v_pk_mul_f32 v[32:33], v[32:33], s[100:101] op_sel:[0,1] op_sel_hi:[1,1]
	v_cvt_pk_fp8_f32 v10, v18, v19
	v_cvt_pk_fp8_f32 v12, v26, v27
	v_cvt_pk_fp8_f32 v10, v20, v21 op_sel:[0,0,1]
	v_cvt_pk_fp8_f32 v12, v28, v29 op_sel:[0,0,1]
	v_cvt_pk_fp8_f32 v11, v22, v23
	v_cvt_pk_fp8_f32 v13, v30, v31
	v_cvt_pk_fp8_f32 v11, v24, v25 op_sel:[0,0,1]
	v_cvt_pk_fp8_f32 v13, v32, v33 op_sel:[0,0,1]
	s_nop 0
	global_store_dwordx2 v[6:7], v[10:11], off
	global_store_dwordx2 v[46:47], v[12:13], off
	s_cbranch_vccnz .LBB0_1010
